# baseline (speedup 1.0000x reference)
.LBB1_3:
	s_mul_i32 s0, s7, s2
	s_sub_i32 s0, s6, s0
	s_add_i32 s1, s7, 1
	s_sub_i32 s6, s0, s2
	s_cmp_ge_u32 s0, s2
	s_cselect_b32 s1, s1, s7
	s_cselect_b32 s0, s6, s0
	s_add_i32 s6, s1, 1
	s_cmp_ge_u32 s0, s2
	s_cselect_b32 s0, s6, s1
	s_xor_b32 s0, s0, s5
	s_sub_i32 s0, s0, s5
	s_mul_i32 s79, s0, s76
	s_add_i32 s0, s79, s0
	s_lshl_b32 s33, s59, 7
	s_add_i32 s4, s33, s4
	s_min_i32 s80, s0, s3
	s_mul_i32 s0, s72, 0x4080
	s_mul_hi_i32 s1, s72, 0x4080
	s_add_u32 s0, s62, s0
	s_addc_u32 s1, s63, s1
	s_mul_i32 s2, s79, 0x4080
	v_and_b32_e32 v114, 63, v0
	s_mul_hi_i32 s3, s79, 0x4080
	s_add_u32 s2, s0, s2
	s_addc_u32 s3, s1, s3
	v_lshlrev_b32_e32 v108, 4, v114
	v_lshl_add_u64 v[2:3], s[2:3], 0, v[108:109]
	s_ashr_i32 s2, s4, 5
	s_mul_hi_i32 s3, s2, 0x4080
	s_mulk_i32 s2, 0x4080
	v_lshrrev_b32_e32 v27, 6, v0
	s_add_u32 s2, s62, s2
	s_addc_u32 s3, s63, s3
	v_lshlrev_b32_e32 v6, 10, v27
	v_lshl_add_u64 v[4:5], s[2:3], 0, v[108:109]
	v_mov_b32_e32 v7, v109
	v_lshl_add_u64 v[8:9], v[2:3], 0, v[6:7]
	v_lshl_add_u64 v[10:11], v[4:5], 0, v[6:7]
	v_add_u32_e32 v14, 0x3000, v6
	v_add_u32_e32 v16, 0x6000, v6
	v_add_u32_e32 v18, 0x9000, v6
	v_bfe_u32 v119, v0, 6, 2
	v_and_b32_e32 v118, 31, v0
	s_mov_b64 s[62:63], 0xc00
	v_add_u32_e32 v15, 0x15000, v6
	s_mov_b64 s[2:3], 0xc00
	v_lshl_add_u64 v[12:13], v[10:11], 0, s[2:3]
	v_readfirstlane_b32 s4, v15
	s_mov_b32 m0, s4
	s_nop 0
	global_load_lds_dwordx4 v[12:13], off
	v_add_u32_e32 v15, 0x18000, v6
	s_mov_b64 s[2:3], 0x3c00
	v_lshl_add_u64 v[12:13], v[10:11], 0, s[2:3]
	v_readfirstlane_b32 s4, v15
	s_mov_b32 m0, s4
	s_nop 0
	global_load_lds_dwordx4 v[12:13], off
	v_add_u32_e32 v15, 0x1b000, v6
	s_mov_b64 s[2:3], 0x6c00
	v_lshl_add_u64 v[12:13], v[10:11], 0, s[2:3]
	v_readfirstlane_b32 s4, v15
	s_mov_b32 m0, s4
	s_nop 0
	global_load_lds_dwordx4 v[12:13], off
	v_add_u32_e32 v15, 0x1e000, v6
	s_mov_b64 s[2:3], 0x9c00
	v_lshl_add_u64 v[12:13], v[10:11], 0, s[2:3]
	v_readfirstlane_b32 s4, v15
	s_mov_b32 m0, s4
	s_nop 0
	global_load_lds_dwordx4 v[12:13], off
	v_add_u32_e32 v15, 0x21000, v6
	s_mov_b64 s[2:3], 0xcc00
	v_lshl_add_u64 v[12:13], v[10:11], 0, s[2:3]
	v_readfirstlane_b32 s4, v15
	s_mov_b32 m0, s4
	s_nop 0
	global_load_lds_dwordx4 v[12:13], off
	v_or_b32_e32 v12, 0x90, v27
	v_min_u32_e32 v12, 0x91, v12
	v_lshlrev_b32_e32 v12, 10, v12
	v_mov_b32_e32 v13, v109
	s_nop 0
	v_readfirstlane_b32 s4, v12
	v_lshl_add_u64 v[12:13], v[4:5], 0, v[12:13]
	s_mov_b32 s2, 0xfffebc00
	s_mov_b32 s3, -1
	v_lshl_add_u64 v[12:13], v[12:13], 0, s[2:3]
	s_mov_b32 m0, s4
	s_nop 0
	global_load_lds_dwordx4 v[12:13], off
	s_movk_i32 s2, 0xdc00
	s_mov_b32 s3, -1
	v_lshl_add_u64 v[12:13], v[10:11], 0, s[2:3]
	s_mov_b64 s[2:3], 0x12000
	v_lshl_add_u64 v[142:143], v[8:9], 0, s[2:3]
	s_movk_i32 s4, 0x23f
	v_cmp_lt_u32_e32 vcc, s4, v0
	v_add_u32_e32 v15, 0x12000, v6
	s_nop 0
	v_cndmask_b32_e32 v12, v142, v12, vcc
	v_cndmask_b32_e32 v13, v143, v13, vcc
	v_readfirstlane_b32 s4, v15
	s_mov_b32 m0, s4
	s_nop 0
	global_load_lds_dwordx4 v[12:13], off
	v_mov_b32_e32 v15, v6
	v_mov_b32_e32 v12, v8
	v_mov_b32_e32 v13, v9
	v_readfirstlane_b32 s4, v15
	s_mov_b32 m0, s4
	s_nop 0
	global_load_lds_dwordx4 v[12:13], off
	v_add_u32_e32 v15, 0x3000, v6
	s_mov_b64 s[2:3], 0x3000
	v_lshl_add_u64 v[12:13], v[8:9], 0, s[2:3]
	v_readfirstlane_b32 s4, v15
	s_mov_b32 m0, s4
	s_nop 0
	global_load_lds_dwordx4 v[12:13], off
	v_add_u32_e32 v15, 0x6000, v6
	s_mov_b64 s[2:3], 0x6000
	v_lshl_add_u64 v[12:13], v[8:9], 0, s[2:3]
	v_readfirstlane_b32 s4, v15
	s_mov_b32 m0, s4
	s_nop 0
	global_load_lds_dwordx4 v[12:13], off
	v_add_u32_e32 v15, 0x9000, v6
	s_mov_b64 s[2:3], 0x9000
	v_lshl_add_u64 v[12:13], v[8:9], 0, s[2:3]
	v_readfirstlane_b32 s4, v15
	s_mov_b32 m0, s4
	s_nop 0
	global_load_lds_dwordx4 v[12:13], off
	v_add_u32_e32 v15, 0xc000, v6
	s_mov_b64 s[2:3], 0xc000
	v_lshl_add_u64 v[12:13], v[8:9], 0, s[2:3]
	v_readfirstlane_b32 s4, v15
	s_mov_b32 m0, s4
	s_nop 0
	global_load_lds_dwordx4 v[12:13], off
	v_add_u32_e32 v15, 0xf000, v6
	s_mov_b64 s[2:3], 0xf000
	v_lshl_add_u64 v[12:13], v[8:9], 0, s[2:3]
	v_readfirstlane_b32 s4, v15
	s_mov_b32 m0, s4
	s_nop 0
	global_load_lds_dwordx4 v[12:13], off
	s_mov_b32 s2, 0x14400
	s_and_b64 vcc, exec, s[68:69]
	s_cbranch_vccz .Lec_skip
	s_waitcnt vmcnt(13)
	v_sub_u32_e32 v142, s78, v115
	v_cmp_lt_i32_e32 vcc, 0, v142
	v_add_f32_e32 v143, 0, v120
	s_nop 0
	v_cndmask_b32_e32 v143, 0, v143, vcc
	v_cmp_lt_i32_e32 vcc, 3, v142
	s_nop 1
	v_cndmask_b32_e32 v144, 0, v121, vcc
	v_add_f32_e32 v143, v143, v144
	v_cmp_lt_i32_e32 vcc, 6, v142
	s_nop 1
	v_cndmask_b32_e32 v144, 0, v122, vcc
	v_add_f32_e32 v143, v143, v144
	v_cmp_lt_i32_e32 vcc, 9, v142
	s_nop 1
	v_cndmask_b32_e32 v144, 0, v123, vcc
	v_add_f32_e32 v143, v143, v144
	v_cmp_lt_i32_e32 vcc, 12, v142
	s_nop 1
	v_cndmask_b32_e32 v144, 0, v124, vcc
	v_add_f32_e32 v143, v143, v144
	v_cmp_lt_i32_e32 vcc, 15, v142
	s_nop 1
	v_cndmask_b32_e32 v144, 0, v125, vcc
	v_add_f32_e32 v143, v143, v144
	v_cmp_lt_i32_e32 vcc, 18, v142
	s_nop 1
	v_cndmask_b32_e32 v144, 0, v126, vcc
	v_add_f32_e32 v143, v143, v144
	v_cmp_lt_i32_e32 vcc, 21, v142
	s_nop 1
	v_cndmask_b32_e32 v144, 0, v127, vcc
	v_add_f32_e32 v143, v143, v144
	v_cmp_lt_i32_e32 vcc, 24, v142
	s_nop 1
	v_cndmask_b32_e32 v144, 0, v128, vcc
	v_add_f32_e32 v143, v143, v144
	v_cmp_lt_i32_e32 vcc, 27, v142
	s_nop 1
	v_cndmask_b32_e32 v144, 0, v129, vcc
	v_add_f32_e32 v143, v143, v144
	v_cmp_lt_i32_e32 vcc, 30, v142
	s_nop 1
	v_cndmask_b32_e32 v144, 0, v130, vcc
	v_add_f32_e32 v143, v143, v144
	v_add_u32_e32 v145, 33, v115
	v_cmp_gt_i32_e32 vcc, s78, v145
	s_and_saveexec_b64 s[84:85], vcc
	s_cbranch_execz .Lec_norare
	v_add_u32_e32 v146, s72, v145
	v_ashrrev_i32_e32 v147, 31, v146
	v_lshlrev_b64 v[146:147], 10, v[146:147]
	v_lshl_or_b32 v146, v1, 2, v146
	v_lshl_add_u64 v[146:147], s[60:61], 0, v[146:147]
	s_mov_b64 s[86:87], 0
.Lec_rare:
	global_load_dword v148, v[146:147], off
	v_add_u32_e32 v145, 3, v145
	v_cmp_le_i32_e32 vcc, s78, v145
	v_lshl_add_u64 v[146:147], v[146:147], 0, s[62:63]
	s_or_b64 s[86:87], vcc, s[86:87]
	s_waitcnt vmcnt(0)
	v_add_f32_e32 v143, v143, v148
	s_andn2_b64 exec, exec, s[86:87]
	s_cbranch_execnz .Lec_rare
.Lec_norare:
	s_mov_b64 exec, s[84:85]
	v_mov_b32_e32 v144, 0x24800
	v_lshl_add_u32 v144, v0, 2, v144
	ds_write_b32 v144, v143
	s_waitcnt lgkmcnt(0)
	s_barrier
	s_movk_i32 s84, 0x100
	v_cmp_gt_u32_e32 vcc, s84, v0
	s_and_saveexec_b64 s[84:85], vcc
	s_cbranch_execz .Lec_cdone
	ds_read2st64_b32 v[146:147], v144 offset1:4
	ds_read_b32 v148, v144 offset:2048
	s_bfe_u32 s88, s77, 0x80008
	s_cmp_lg_u32 s59, 0
	s_waitcnt lgkmcnt(1)
	v_add_f32_e32 v146, v146, v147
	s_waitcnt lgkmcnt(0)
	v_add_f32_e32 v146, v146, v148
	s_cbranch_scc1 .Lec_nostore
	v_lshlrev_b32_e32 v147, 2, v0
	v_lshl_or_b32 v147, s88, 10, v147
	global_store_dword v147, v146, s[64:65]
.Lec_nostore:
	v_cvt_f32_i32_e32 v147, s58
	v_mov_b32_e32 v148, 0x25400
	v_lshl_add_u32 v148, v0, 2, v148
	v_div_scale_f32 v149, s[86:87], v147, v147, v146
	v_rcp_f32_e32 v150, v149
	v_div_scale_f32 v151, vcc, v146, v147, v146
	v_fma_f32 v152, -v149, v150, 1.0
	v_fmac_f32_e32 v150, v152, v150
	v_mul_f32_e32 v152, v151, v150
	v_fma_f32 v153, -v149, v152, v151
	v_fmac_f32_e32 v152, v153, v150
	v_fma_f32 v149, -v149, v152, v151
	v_div_fmas_f32 v149, v149, v150, v152
	v_div_fixup_f32 v146, v149, v147, v146
	v_mul_f32_e32 v147, v146, v146
	ds_write_b32 v148, v146
	v_cmp_eq_u32_e32 vcc, 0, v114
	v_mov_b32_dpp v147, v147 quad_perm:[1,0,3,2] row_mask:0xf bank_mask:0xf bound_ctrl:1
	v_fmac_f32_e32 v147, v146, v146
	s_nop 1
	v_add_f32_dpp v146, v147, v147 quad_perm:[2,3,0,1] row_mask:0xf bank_mask:0xf bound_ctrl:1
	s_nop 1
	v_add_f32_dpp v146, v146, v146 row_half_mirror row_mask:0xf bank_mask:0xf bound_ctrl:1
	s_nop 1
	v_add_f32_dpp v146, v146, v146 row_mirror row_mask:0xf bank_mask:0xf bound_ctrl:1
	s_nop 0
	v_readlane_b32 s88, v146, 0
	v_readlane_b32 s90, v146, 16
	v_readlane_b32 s89, v146, 32
	v_readlane_b32 s91, v146, 48
	s_and_b64 exec, exec, vcc
	s_cbranch_execz .Lec_cdone
	v_mov_b32_e32 v146, 0x25830
	v_lshl_add_u32 v148, v27, 2, v146
	v_mov_b32_e32 v146, s90
	v_mov_b32_e32 v147, s91
	v_pk_add_f32 v[146:147], s[88:89], v[146:147]
	s_nop 0
	v_add_f32_e32 v146, v146, v147
	ds_write_b32 v148, v146
.Lec_cdone:
	s_mov_b64 exec, s[84:85]
.Lec_skip:
	v_mul_u32_u24_e32 v4, 0x4080, v119
	s_waitcnt vmcnt(6)
	v_add3_u32 v5, v108, v4, s2
	v_lshl_or_b32 v4, v118, 2, v4
	s_mov_b64 s[2:3], 0x14280
	s_waitcnt lgkmcnt(0)
	s_barrier
	v_add_u32_e32 v4, 0x18400, v4
	v_lshl_add_u64 v[2:3], v[2:3], 0, s[2:3]
	ds_read_b128 v[88:91], v5
	ds_read_b128 v[84:87], v5 offset:1024
	ds_read_b128 v[80:83], v5 offset:2048
	ds_read_b128 v[76:79], v5 offset:3072
	ds_read_b128 v[72:75], v5 offset:4096
	ds_read_b128 v[68:71], v5 offset:5120
	ds_read_b128 v[64:67], v5 offset:6144
	ds_read_b128 v[60:63], v5 offset:7168
	ds_read_b128 v[56:59], v5 offset:8192
	ds_read_b128 v[52:55], v5 offset:9216
	ds_read_b128 v[48:51], v5 offset:10240
	ds_read_b128 v[44:47], v5 offset:11264
	ds_read_b128 v[40:43], v5 offset:12288
	ds_read_b128 v[36:39], v5 offset:13312
	ds_read_b128 v[32:35], v5 offset:14336
	ds_read_b128 v[28:31], v5 offset:15360
	ds_read_b32 v116, v4
	s_waitcnt lgkmcnt(0)
	v_lshl_add_u64 v[4:5], v[2:3], 0, v[6:7]
	v_add_u32_e32 v7, 0x14280, v6
	s_barrier
	v_readfirstlane_b32 s2, v7
	v_add_u32_e32 v7, 0x17280, v6
	s_mov_b32 m0, s2
	v_mov_b32_e32 v15, v109
	v_readfirstlane_b32 s2, v7
	v_add_u32_e32 v7, 0x1a280, v6
	global_load_lds_dwordx4 v[4:5], off
	v_lshl_add_u64 v[4:5], v[2:3], 0, v[14:15]
	s_mov_b32 m0, s2
	v_mov_b32_e32 v17, v109
	v_readfirstlane_b32 s2, v7
	v_add_u32_e32 v7, 0x1d280, v6
	global_load_lds_dwordx4 v[4:5], off
	v_lshl_add_u64 v[4:5], v[2:3], 0, v[16:17]
	s_mov_b32 m0, s2
	v_mov_b32_e32 v19, v109
	v_readfirstlane_b32 s2, v7
	global_load_lds_dwordx4 v[4:5], off
	v_lshl_add_u64 v[4:5], v[2:3], 0, v[18:19]
	s_mov_b32 m0, s2
	v_bfe_u32 v117, v0, 5, 1
	global_load_lds_dwordx4 v[4:5], off
	v_or_b32_e32 v4, 0xc000, v6
	v_add_u32_e32 v6, 0x20280, v6
	v_mov_b32_e32 v5, v109
	v_readfirstlane_b32 s2, v6
	v_lshl_add_u64 v[4:5], v[2:3], 0, v[4:5]
	s_mov_b32 m0, s2
	v_add_u32_e32 v131, 33, v115
	global_load_lds_dwordx4 v[4:5], off
	v_min_u32_e32 v4, 4, v27
	v_lshlrev_b32_e32 v6, 10, v4
	v_add_u32_e32 v4, 0xf000, v6
	v_mov_b32_e32 v5, v109
	v_lshl_add_u64 v[2:3], v[2:3], 0, v[4:5]
	v_add_u32_e32 v4, 0x23280, v6
	s_movk_i32 s73, 0x4080
	v_readfirstlane_b32 s2, v4
	s_mov_b32 m0, s2
	v_mov_b32_e32 v18, 0x7f800000
	global_load_lds_dwordx4 v[2:3], off
	v_lshrrev_b32_e32 v2, 1, v0
	v_and_b32_e32 v3, 3, v0
	v_and_or_b32 v2, v2, 12, v3
	v_cmp_eq_u32_e64 s[2:3], 0, v2
	v_cmp_eq_u32_e64 s[4:5], 1, v2
	v_cmp_eq_u32_e64 s[6:7], 2, v2
	v_cmp_eq_u32_e64 s[8:9], 3, v2
	v_cmp_eq_u32_e64 s[10:11], 4, v2
	v_cmp_eq_u32_e64 s[12:13], 5, v2
	v_cmp_eq_u32_e64 s[14:15], 6, v2
	v_cmp_eq_u32_e64 s[16:17], 7, v2
	v_cmp_eq_u32_e64 s[18:19], 8, v2
	v_cmp_eq_u32_e64 s[20:21], 9, v2
	v_cmp_eq_u32_e64 s[22:23], 10, v2
	v_cmp_eq_u32_e64 s[24:25], 11, v2
	v_cmp_eq_u32_e64 s[26:27], 12, v2
	v_cmp_eq_u32_e64 s[28:29], 13, v2
	v_cmp_eq_u32_e64 s[30:31], 14, v2
	v_cmp_eq_u32_e64 s[34:35], 15, v2
	v_mul_u32_u24_e32 v2, 0x4080, v115
	v_lshl_or_b32 v2, v117, 4, v2
	v_bfe_u32 v3, v0, 2, 1
	v_add_u32_e32 v132, 0x4000, v2
	v_lshl_or_b32 v2, s59, 2, v119
	v_cmp_eq_u32_e32 vcc, v117, v3
	v_sub_u32_e32 v3, s78, v115
	v_sub_u32_e32 v134, v2, v115
	v_add_u32_e32 v2, s72, v131
	v_cmp_lt_i32_e64 s[36:37], 0, v3
	v_cmp_lt_i32_e64 s[38:39], 3, v3
	v_cmp_lt_i32_e64 s[40:41], 6, v3
	v_cmp_lt_i32_e64 s[42:43], 9, v3
	v_cmp_lt_i32_e64 s[44:45], 12, v3
	v_cmp_lt_i32_e64 s[46:47], 15, v3
	v_cmp_lt_i32_e64 s[48:49], 18, v3
	v_cmp_lt_i32_e64 s[50:51], 21, v3
	v_cmp_lt_i32_e64 s[52:53], 24, v3
	v_cmp_lt_i32_e64 s[54:55], 27, v3
	v_cmp_lt_i32_e64 s[56:57], 30, v3
	v_ashrrev_i32_e32 v3, 31, v2
	v_lshlrev_b64 v[2:3], 10, v[2:3]
	v_lshl_or_b32 v2, v1, 2, v2
	v_lshl_add_u64 v[110:111], s[0:1], 0, v[108:109]
	v_cmp_gt_i32_e64 s[0:1], s78, v131
	s_and_b64 s[2:3], vcc, s[2:3]
	s_and_b64 s[4:5], vcc, s[4:5]
	s_and_b64 s[6:7], vcc, s[6:7]
	s_and_b64 s[8:9], vcc, s[8:9]
	s_and_b64 s[10:11], vcc, s[10:11]
	s_and_b64 s[12:13], vcc, s[12:13]
	s_and_b64 s[14:15], vcc, s[14:15]
	s_and_b64 s[16:17], vcc, s[16:17]
	s_and_b64 s[18:19], vcc, s[18:19]
	s_and_b64 s[20:21], vcc, s[20:21]
	s_and_b64 s[22:23], vcc, s[22:23]
	s_and_b64 s[24:25], vcc, s[24:25]
	s_and_b64 s[26:27], vcc, s[26:27]
	s_and_b64 s[28:29], vcc, s[28:29]
	s_and_b64 s[30:31], vcc, s[30:31]
	s_and_b64 s[34:35], vcc, s[34:35]
	v_mad_u32_u24 v133, v115, s73, v108
	v_lshl_add_u64 v[112:113], s[60:61], 0, v[2:3]
	s_mov_b64 s[60:61], -1
	v_mov_b32_e32 v135, 0x4080
	v_mov_b32_e32 v136, 0xff800000
	v_mov_b32_e32 v137, 0
	s_mov_b32 s81, s79
	v_mov_b32_e32 v1, v18
	v_mov_b32_e32 v20, v18
	v_mov_b32_e32 v19, v18
	v_mov_b32_e32 v24, v18
	v_mov_b32_e32 v23, v18
	v_mov_b32_e32 v22, v18
	v_mov_b32_e32 v21, v18
	v_mov_b32_e32 v26, v18
	v_mov_b32_e32 v25, v18
	s_and_b64 vcc, exec, s[68:69]
	s_cbranch_vccz .Led_skip
	v_readfirstlane_b32 s84, v115
	s_cmp_lg_u32 s84, 1
	s_cbranch_scc1 .Led_skip
	v_and_b32_e32 v14, 32, v0
	v_or_b32_e32 v15, 0x25400, v14
	v_mov_b32_e32 v2, 0
	v_mov_b32_e32 v3, 0
	v_mov_b32_e32 v4, 0
	v_mov_b32_e32 v5, 0
	ds_read_b128 v[92:95], v15 offset:0
	ds_read_b128 v[96:99], v15 offset:16
	ds_read_b128 v[100:103], v15 offset:64
	ds_read_b128 v[104:107], v15 offset:80
	ds_read_b128 v[142:145], v15 offset:128
	ds_read_b128 v[146:149], v15 offset:144
	ds_read_b128 v[150:153], v15 offset:192
	ds_read_b128 v[154:157], v15 offset:208
	s_waitcnt lgkmcnt(0)
	v_fma_mix_f32 v2, v88, v92, v2 op_sel:[0,0,0] op_sel_hi:[1,0,0]
	v_fma_mix_f32 v3, v84, v100, v3 op_sel:[0,0,0] op_sel_hi:[1,0,0]
	v_fma_mix_f32 v4, v80, v142, v4 op_sel:[0,0,0] op_sel_hi:[1,0,0]
	v_fma_mix_f32 v5, v76, v150, v5 op_sel:[0,0,0] op_sel_hi:[1,0,0]
	v_fma_mix_f32 v2, v88, v93, v2 op_sel:[1,0,0] op_sel_hi:[1,0,0]
	v_fma_mix_f32 v3, v84, v101, v3 op_sel:[1,0,0] op_sel_hi:[1,0,0]
	v_fma_mix_f32 v4, v80, v143, v4 op_sel:[1,0,0] op_sel_hi:[1,0,0]
	v_fma_mix_f32 v5, v76, v151, v5 op_sel:[1,0,0] op_sel_hi:[1,0,0]
	v_fma_mix_f32 v2, v89, v94, v2 op_sel:[0,0,0] op_sel_hi:[1,0,0]
	v_fma_mix_f32 v3, v85, v102, v3 op_sel:[0,0,0] op_sel_hi:[1,0,0]
	v_fma_mix_f32 v4, v81, v144, v4 op_sel:[0,0,0] op_sel_hi:[1,0,0]
	v_fma_mix_f32 v5, v77, v152, v5 op_sel:[0,0,0] op_sel_hi:[1,0,0]
	v_fma_mix_f32 v2, v89, v95, v2 op_sel:[1,0,0] op_sel_hi:[1,0,0]
	v_fma_mix_f32 v3, v85, v103, v3 op_sel:[1,0,0] op_sel_hi:[1,0,0]
	v_fma_mix_f32 v4, v81, v145, v4 op_sel:[1,0,0] op_sel_hi:[1,0,0]
	v_fma_mix_f32 v5, v77, v153, v5 op_sel:[1,0,0] op_sel_hi:[1,0,0]
	v_fma_mix_f32 v2, v90, v96, v2 op_sel:[0,0,0] op_sel_hi:[1,0,0]
	v_fma_mix_f32 v3, v86, v104, v3 op_sel:[0,0,0] op_sel_hi:[1,0,0]
	v_fma_mix_f32 v4, v82, v146, v4 op_sel:[0,0,0] op_sel_hi:[1,0,0]
	v_fma_mix_f32 v5, v78, v154, v5 op_sel:[0,0,0] op_sel_hi:[1,0,0]
	v_fma_mix_f32 v2, v90, v97, v2 op_sel:[1,0,0] op_sel_hi:[1,0,0]
	v_fma_mix_f32 v3, v86, v105, v3 op_sel:[1,0,0] op_sel_hi:[1,0,0]
	v_fma_mix_f32 v4, v82, v147, v4 op_sel:[1,0,0] op_sel_hi:[1,0,0]
	v_fma_mix_f32 v5, v78, v155, v5 op_sel:[1,0,0] op_sel_hi:[1,0,0]
	v_fma_mix_f32 v2, v91, v98, v2 op_sel:[0,0,0] op_sel_hi:[1,0,0]
	v_fma_mix_f32 v3, v87, v106, v3 op_sel:[0,0,0] op_sel_hi:[1,0,0]
	v_fma_mix_f32 v4, v83, v148, v4 op_sel:[0,0,0] op_sel_hi:[1,0,0]
	v_fma_mix_f32 v5, v79, v156, v5 op_sel:[0,0,0] op_sel_hi:[1,0,0]
	v_fma_mix_f32 v2, v91, v99, v2 op_sel:[1,0,0] op_sel_hi:[1,0,0]
	v_fma_mix_f32 v3, v87, v107, v3 op_sel:[1,0,0] op_sel_hi:[1,0,0]
	v_fma_mix_f32 v4, v83, v149, v4 op_sel:[1,0,0] op_sel_hi:[1,0,0]
	v_fma_mix_f32 v5, v79, v157, v5 op_sel:[1,0,0] op_sel_hi:[1,0,0]
	ds_read_b128 v[92:95], v15 offset:256
	ds_read_b128 v[96:99], v15 offset:272
	ds_read_b128 v[100:103], v15 offset:320
	ds_read_b128 v[104:107], v15 offset:336
	ds_read_b128 v[142:145], v15 offset:384
	ds_read_b128 v[146:149], v15 offset:400
	ds_read_b128 v[150:153], v15 offset:448
	ds_read_b128 v[154:157], v15 offset:464
	s_waitcnt lgkmcnt(0)
	v_fma_mix_f32 v2, v72, v92, v2 op_sel:[0,0,0] op_sel_hi:[1,0,0]
	v_fma_mix_f32 v3, v68, v100, v3 op_sel:[0,0,0] op_sel_hi:[1,0,0]
	v_fma_mix_f32 v4, v64, v142, v4 op_sel:[0,0,0] op_sel_hi:[1,0,0]
	v_fma_mix_f32 v5, v60, v150, v5 op_sel:[0,0,0] op_sel_hi:[1,0,0]
	v_fma_mix_f32 v2, v72, v93, v2 op_sel:[1,0,0] op_sel_hi:[1,0,0]
	v_fma_mix_f32 v3, v68, v101, v3 op_sel:[1,0,0] op_sel_hi:[1,0,0]
	v_fma_mix_f32 v4, v64, v143, v4 op_sel:[1,0,0] op_sel_hi:[1,0,0]
	v_fma_mix_f32 v5, v60, v151, v5 op_sel:[1,0,0] op_sel_hi:[1,0,0]
	v_fma_mix_f32 v2, v73, v94, v2 op_sel:[0,0,0] op_sel_hi:[1,0,0]
	v_fma_mix_f32 v3, v69, v102, v3 op_sel:[0,0,0] op_sel_hi:[1,0,0]
	v_fma_mix_f32 v4, v65, v144, v4 op_sel:[0,0,0] op_sel_hi:[1,0,0]
	v_fma_mix_f32 v5, v61, v152, v5 op_sel:[0,0,0] op_sel_hi:[1,0,0]
	v_fma_mix_f32 v2, v73, v95, v2 op_sel:[1,0,0] op_sel_hi:[1,0,0]
	v_fma_mix_f32 v3, v69, v103, v3 op_sel:[1,0,0] op_sel_hi:[1,0,0]
	v_fma_mix_f32 v4, v65, v145, v4 op_sel:[1,0,0] op_sel_hi:[1,0,0]
	v_fma_mix_f32 v5, v61, v153, v5 op_sel:[1,0,0] op_sel_hi:[1,0,0]
	v_fma_mix_f32 v2, v74, v96, v2 op_sel:[0,0,0] op_sel_hi:[1,0,0]
	v_fma_mix_f32 v3, v70, v104, v3 op_sel:[0,0,0] op_sel_hi:[1,0,0]
	v_fma_mix_f32 v4, v66, v146, v4 op_sel:[0,0,0] op_sel_hi:[1,0,0]
	v_fma_mix_f32 v5, v62, v154, v5 op_sel:[0,0,0] op_sel_hi:[1,0,0]
	v_fma_mix_f32 v2, v74, v97, v2 op_sel:[1,0,0] op_sel_hi:[1,0,0]
	v_fma_mix_f32 v3, v70, v105, v3 op_sel:[1,0,0] op_sel_hi:[1,0,0]
	v_fma_mix_f32 v4, v66, v147, v4 op_sel:[1,0,0] op_sel_hi:[1,0,0]
	v_fma_mix_f32 v5, v62, v155, v5 op_sel:[1,0,0] op_sel_hi:[1,0,0]
	v_fma_mix_f32 v2, v75, v98, v2 op_sel:[0,0,0] op_sel_hi:[1,0,0]
	v_fma_mix_f32 v3, v71, v106, v3 op_sel:[0,0,0] op_sel_hi:[1,0,0]
	v_fma_mix_f32 v4, v67, v148, v4 op_sel:[0,0,0] op_sel_hi:[1,0,0]
	v_fma_mix_f32 v5, v63, v156, v5 op_sel:[0,0,0] op_sel_hi:[1,0,0]
	v_fma_mix_f32 v2, v75, v99, v2 op_sel:[1,0,0] op_sel_hi:[1,0,0]
	v_fma_mix_f32 v3, v71, v107, v3 op_sel:[1,0,0] op_sel_hi:[1,0,0]
	v_fma_mix_f32 v4, v67, v149, v4 op_sel:[1,0,0] op_sel_hi:[1,0,0]
	v_fma_mix_f32 v5, v63, v157, v5 op_sel:[1,0,0] op_sel_hi:[1,0,0]
	ds_read_b128 v[92:95], v15 offset:512
	ds_read_b128 v[96:99], v15 offset:528
	ds_read_b128 v[100:103], v15 offset:576
	ds_read_b128 v[104:107], v15 offset:592
	ds_read_b128 v[142:145], v15 offset:640
	ds_read_b128 v[146:149], v15 offset:656
	ds_read_b128 v[150:153], v15 offset:704
	ds_read_b128 v[154:157], v15 offset:720
	s_waitcnt lgkmcnt(0)
	v_fma_mix_f32 v2, v56, v92, v2 op_sel:[0,0,0] op_sel_hi:[1,0,0]
	v_fma_mix_f32 v3, v52, v100, v3 op_sel:[0,0,0] op_sel_hi:[1,0,0]
	v_fma_mix_f32 v4, v48, v142, v4 op_sel:[0,0,0] op_sel_hi:[1,0,0]
	v_fma_mix_f32 v5, v44, v150, v5 op_sel:[0,0,0] op_sel_hi:[1,0,0]
	v_fma_mix_f32 v2, v56, v93, v2 op_sel:[1,0,0] op_sel_hi:[1,0,0]
	v_fma_mix_f32 v3, v52, v101, v3 op_sel:[1,0,0] op_sel_hi:[1,0,0]
	v_fma_mix_f32 v4, v48, v143, v4 op_sel:[1,0,0] op_sel_hi:[1,0,0]
	v_fma_mix_f32 v5, v44, v151, v5 op_sel:[1,0,0] op_sel_hi:[1,0,0]
	v_fma_mix_f32 v2, v57, v94, v2 op_sel:[0,0,0] op_sel_hi:[1,0,0]
	v_fma_mix_f32 v3, v53, v102, v3 op_sel:[0,0,0] op_sel_hi:[1,0,0]
	v_fma_mix_f32 v4, v49, v144, v4 op_sel:[0,0,0] op_sel_hi:[1,0,0]
	v_fma_mix_f32 v5, v45, v152, v5 op_sel:[0,0,0] op_sel_hi:[1,0,0]
	v_fma_mix_f32 v2, v57, v95, v2 op_sel:[1,0,0] op_sel_hi:[1,0,0]
	v_fma_mix_f32 v3, v53, v103, v3 op_sel:[1,0,0] op_sel_hi:[1,0,0]
	v_fma_mix_f32 v4, v49, v145, v4 op_sel:[1,0,0] op_sel_hi:[1,0,0]
	v_fma_mix_f32 v5, v45, v153, v5 op_sel:[1,0,0] op_sel_hi:[1,0,0]
	v_fma_mix_f32 v2, v58, v96, v2 op_sel:[0,0,0] op_sel_hi:[1,0,0]
	v_fma_mix_f32 v3, v54, v104, v3 op_sel:[0,0,0] op_sel_hi:[1,0,0]
	v_fma_mix_f32 v4, v50, v146, v4 op_sel:[0,0,0] op_sel_hi:[1,0,0]
	v_fma_mix_f32 v5, v46, v154, v5 op_sel:[0,0,0] op_sel_hi:[1,0,0]
	v_fma_mix_f32 v2, v58, v97, v2 op_sel:[1,0,0] op_sel_hi:[1,0,0]
	v_fma_mix_f32 v3, v54, v105, v3 op_sel:[1,0,0] op_sel_hi:[1,0,0]
	v_fma_mix_f32 v4, v50, v147, v4 op_sel:[1,0,0] op_sel_hi:[1,0,0]
	v_fma_mix_f32 v5, v46, v155, v5 op_sel:[1,0,0] op_sel_hi:[1,0,0]
	v_fma_mix_f32 v2, v59, v98, v2 op_sel:[0,0,0] op_sel_hi:[1,0,0]
	v_fma_mix_f32 v3, v55, v106, v3 op_sel:[0,0,0] op_sel_hi:[1,0,0]
	v_fma_mix_f32 v4, v51, v148, v4 op_sel:[0,0,0] op_sel_hi:[1,0,0]
	v_fma_mix_f32 v5, v47, v156, v5 op_sel:[0,0,0] op_sel_hi:[1,0,0]
	v_fma_mix_f32 v2, v59, v99, v2 op_sel:[1,0,0] op_sel_hi:[1,0,0]
	v_fma_mix_f32 v3, v55, v107, v3 op_sel:[1,0,0] op_sel_hi:[1,0,0]
	v_fma_mix_f32 v4, v51, v149, v4 op_sel:[1,0,0] op_sel_hi:[1,0,0]
	v_fma_mix_f32 v5, v47, v157, v5 op_sel:[1,0,0] op_sel_hi:[1,0,0]
	ds_read_b128 v[92:95], v15 offset:768
	ds_read_b128 v[96:99], v15 offset:784
	ds_read_b128 v[100:103], v15 offset:832
	ds_read_b128 v[104:107], v15 offset:848
	ds_read_b128 v[142:145], v15 offset:896
	ds_read_b128 v[146:149], v15 offset:912
	ds_read_b128 v[150:153], v15 offset:960
	ds_read_b128 v[154:157], v15 offset:976
	s_waitcnt lgkmcnt(0)
	v_fma_mix_f32 v2, v40, v92, v2 op_sel:[0,0,0] op_sel_hi:[1,0,0]
	v_fma_mix_f32 v3, v36, v100, v3 op_sel:[0,0,0] op_sel_hi:[1,0,0]
	v_fma_mix_f32 v4, v32, v142, v4 op_sel:[0,0,0] op_sel_hi:[1,0,0]
	v_fma_mix_f32 v5, v28, v150, v5 op_sel:[0,0,0] op_sel_hi:[1,0,0]
	v_fma_mix_f32 v2, v40, v93, v2 op_sel:[1,0,0] op_sel_hi:[1,0,0]
	v_fma_mix_f32 v3, v36, v101, v3 op_sel:[1,0,0] op_sel_hi:[1,0,0]
	v_fma_mix_f32 v4, v32, v143, v4 op_sel:[1,0,0] op_sel_hi:[1,0,0]
	v_fma_mix_f32 v5, v28, v151, v5 op_sel:[1,0,0] op_sel_hi:[1,0,0]
	v_fma_mix_f32 v2, v41, v94, v2 op_sel:[0,0,0] op_sel_hi:[1,0,0]
	v_fma_mix_f32 v3, v37, v102, v3 op_sel:[0,0,0] op_sel_hi:[1,0,0]
	v_fma_mix_f32 v4, v33, v144, v4 op_sel:[0,0,0] op_sel_hi:[1,0,0]
	v_fma_mix_f32 v5, v29, v152, v5 op_sel:[0,0,0] op_sel_hi:[1,0,0]
	v_fma_mix_f32 v2, v41, v95, v2 op_sel:[1,0,0] op_sel_hi:[1,0,0]
	v_fma_mix_f32 v3, v37, v103, v3 op_sel:[1,0,0] op_sel_hi:[1,0,0]
	v_fma_mix_f32 v4, v33, v145, v4 op_sel:[1,0,0] op_sel_hi:[1,0,0]
	v_fma_mix_f32 v5, v29, v153, v5 op_sel:[1,0,0] op_sel_hi:[1,0,0]
	v_fma_mix_f32 v2, v42, v96, v2 op_sel:[0,0,0] op_sel_hi:[1,0,0]
	v_fma_mix_f32 v3, v38, v104, v3 op_sel:[0,0,0] op_sel_hi:[1,0,0]
	v_fma_mix_f32 v4, v34, v146, v4 op_sel:[0,0,0] op_sel_hi:[1,0,0]
	v_fma_mix_f32 v5, v30, v154, v5 op_sel:[0,0,0] op_sel_hi:[1,0,0]
	v_fma_mix_f32 v2, v42, v97, v2 op_sel:[1,0,0] op_sel_hi:[1,0,0]
	v_fma_mix_f32 v3, v38, v105, v3 op_sel:[1,0,0] op_sel_hi:[1,0,0]
	v_fma_mix_f32 v4, v34, v147, v4 op_sel:[1,0,0] op_sel_hi:[1,0,0]
	v_fma_mix_f32 v5, v30, v155, v5 op_sel:[1,0,0] op_sel_hi:[1,0,0]
	v_fma_mix_f32 v2, v43, v98, v2 op_sel:[0,0,0] op_sel_hi:[1,0,0]
	v_fma_mix_f32 v3, v39, v106, v3 op_sel:[0,0,0] op_sel_hi:[1,0,0]
	v_fma_mix_f32 v4, v35, v148, v4 op_sel:[0,0,0] op_sel_hi:[1,0,0]
	v_fma_mix_f32 v5, v31, v156, v5 op_sel:[0,0,0] op_sel_hi:[1,0,0]
	v_fma_mix_f32 v2, v43, v99, v2 op_sel:[1,0,0] op_sel_hi:[1,0,0]
	v_fma_mix_f32 v3, v39, v107, v3 op_sel:[1,0,0] op_sel_hi:[1,0,0]
	v_fma_mix_f32 v4, v35, v149, v4 op_sel:[1,0,0] op_sel_hi:[1,0,0]
	v_fma_mix_f32 v5, v31, v157, v5 op_sel:[1,0,0] op_sel_hi:[1,0,0]
	v_add_f32_e32 v2, v2, v3
	v_add_f32_e32 v4, v4, v5
	v_add_f32_e32 v6, v2, v4
	v_mov_b32_e32 v2, 0x25830
	ds_read_b128 v[8:11], v2
	v_lshl_or_b32 v16, v119, 5, v118
	v_or_b32_e32 v16, s33, v16
	s_mov_b32 s84, 0xf800000
	v_cmp_gt_u32_e64 s[90:91], 32, v114
	v_mov_b32_e32 v7, v6
	v_mov_b32_e32 v12, v6
	s_nop 1
	v_permlane32_swap_b32_e32 v7, v12
	v_cmp_eq_u32_e32 vcc, v7, v6
	v_mov_b32_e32 v17, v116
	s_waitcnt lgkmcnt(0)
	v_add_f32_e32 v2, v9, v8
	v_add_f32_e32 v3, v10, v11
	v_cndmask_b32_e32 v7, v7, v12, vcc
	v_add_f32_e32 v6, v6, v7
	v_add_f32_e32 v2, v2, v3
	v_fmac_f32_e32 v17, -2.0, v6
	v_add_f32_e32 v2, v2, v17
	v_max_f32_e32 v2, 0, v2
	v_mul_f32_e32 v3, 0x4f800000, v2
	v_cmp_gt_f32_e32 vcc, s84, v2
	v_cmp_gt_i32_e64 s[86:87], s58, v16
	s_nop 0
	v_cndmask_b32_e32 v2, v2, v3, vcc
	v_sqrt_f32_e32 v3, v2
	s_nop 0
	v_add_u32_e32 v16, -1, v3
	v_fma_f32 v4, -v16, v3, v2
	v_cmp_ge_f32_e64 s[88:89], 0, v4
	v_add_u32_e32 v4, 1, v3
	s_nop 0
	v_cndmask_b32_e64 v16, v3, v16, s[88:89]
	v_fma_f32 v3, -v4, v3, v2
	v_cmp_lt_f32_e64 s[88:89], 0, v3
	s_nop 1
	v_cndmask_b32_e64 v16, v16, v4, s[88:89]
	v_mul_f32_e32 v3, 0x37800000, v16
	v_cndmask_b32_e32 v16, v16, v3, vcc
	v_mov_b32_e32 v3, 0x260
	v_cmp_class_f32_e32 vcc, v2, v3
	s_nop 1
	v_cndmask_b32_e32 v16, v16, v2, vcc
	s_and_b64 vcc, s[86:87], s[90:91]
	v_cndmask_b32_e32 v16, 0, v16, vcc
	s_nop 1
	v_add_f32_dpp v16, v16, v16 quad_perm:[1,0,3,2] row_mask:0xf bank_mask:0xf bound_ctrl:1
	s_nop 1
	v_add_f32_dpp v16, v16, v16 quad_perm:[2,3,0,1] row_mask:0xf bank_mask:0xf bound_ctrl:1
	s_nop 1
	v_add_f32_dpp v16, v16, v16 row_half_mirror row_mask:0xf bank_mask:0xf bound_ctrl:1
	s_nop 1
	v_add_f32_dpp v16, v16, v16 row_mirror row_mask:0xf bank_mask:0xf bound_ctrl:1
	s_nop 0
	v_readlane_b32 s94, v16, 16
	v_readlane_b32 s95, v16, 48
	v_readlane_b32 s92, v16, 0
	v_readlane_b32 s93, v16, 32
	v_mov_b32_e32 v2, s94
	v_mov_b32_e32 v3, s95
	v_pk_add_f32 v[2:3], s[92:93], v[2:3]
	s_nop 0
	v_add_f32_e32 v2, v2, v3
	v_cmp_eq_u32_e32 vcc, 0, v114
	s_and_saveexec_b64 s[84:85], vcc
	v_mov_b32_e32 v3, 0x25800
	v_lshl_add_u32 v3, v27, 2, v3
	ds_write_b32 v3, v2
	s_mov_b64 exec, s[84:85]
.Led_skip:
	s_waitcnt vmcnt(7)
	s_barrier
	s_branch .LBB1_6

.LBB1_28:
	s_movk_i32 s0, 0x100
	v_cmp_gt_u32_e32 vcc, s0, v0
	s_bfe_u32 s8, s77, 0x80008
	s_mov_b64 s[2:3], 0
	s_and_saveexec_b64 s[0:1], s[2:3]
	s_cbranch_execz .LBB1_33
	v_mov_b32_e32 v2, 0x24800
	v_lshl_add_u32 v4, v0, 2, v2
	ds_read2st64_b32 v[2:3], v4 offset1:4
	ds_read_b32 v4, v4 offset:2048
	s_cmp_lg_u32 s59, 0
	s_waitcnt lgkmcnt(1)
	v_add_f32_e32 v2, v2, v3
	s_waitcnt lgkmcnt(0)
	v_add_f32_e32 v2, v2, v4
	s_cbranch_scc1 .LBB1_31
	v_lshlrev_b32_e32 v3, 2, v0
	v_lshl_or_b32 v3, s8, 10, v3
	global_store_dword v3, v2, s[64:65]

.LBB1_39:
	s_or_b64 exec, exec, s[2:3]
	s_andn2_b64 vcc, exec, s[68:69]
	s_cbranch_vccnz .LBB1_46
	v_cmp_eq_u32_e32 vcc, 0, v0
	s_and_saveexec_b64 s[0:1], vcc
	s_cbranch_execz .LBB1_46
	v_mov_b32_e32 v0, 0x25810
	ds_read_b128 v[0:3], v0
	s_lshl_b32 s0, s8, 6
	s_add_i32 s0, s0, s59
	s_ashr_i32 s1, s0, 31
	s_lshl_b64 s[0:1], s[0:1], 2
	s_waitcnt lgkmcnt(0)
	v_add_f32_e32 v0, v0, v1
	v_add_f32_e32 v0, v0, v2
	s_add_u32 s0, s66, s0
	v_add_f32_e32 v0, v0, v3
	s_addc_u32 s1, s67, s1
	v_mov_b32_e32 v1, 0
	global_store_dword v1, v0, s[0:1]
